# gate/up layer 0: next unit's row-map loads no longer followed by vmcnt(0) at the unit top (own registers, post-processing deferred into the K-loop, first three counted waits 12 to 22) + down epilogue
# speedup vs baseline: 1.0124x; 1.0021x over previous
.LBB0_1540:
	s_nop 0
	v_cndmask_b32_e64 v2, 0, 1, s[8:9]
	v_cmp_ne_u32_e64 s[6:7], 1, v2
	s_andn2_b64 vcc, exec, s[8:9]
	v_mov_b32_e32 v148, v150
	v_mov_b32_e32 v146, v152
	v_mov_b32_e32 v170, v154
	v_mov_b32_e32 v169, v142
	s_cbranch_vccnz .LBB0_1542
	s_ashr_i32 s73, s72, 31
	s_lshl_b64 s[76:77], s[72:73], 10
	s_add_u32 s76, s4, s76
	s_addc_u32 s77, s5, s77
	global_load_dword v246, v1, s[76:77]
	global_load_dword v247, v160, s[76:77]
	global_load_dword v248, v160, s[76:77] offset:512
	global_load_dword v249, v1, s[76:77] offset:512
.LBB0_1542:
	ds_read_b128 v[2:5], v165
	ds_read_b128 v[6:9], v165 offset:1024
	ds_read_b128 v[178:181], v165 offset:2048
	ds_read_b128 v[182:185], v165 offset:3072
	ds_read_b128 v[186:189], v166
	ds_read_b128 v[190:193], v166 offset:1024
	ds_read_b128 v[194:197], v166 offset:2048
	ds_read_b128 v[198:201], v166 offset:3072
	s_ashr_i32 s75, s74, 31
	s_ashr_i32 s69, s68, 31
	s_lshl_b64 s[76:77], s[74:75], 21
	s_lshl_b64 s[84:85], s[68:69], 18
	s_add_u32 s69, s1, s76
	s_addc_u32 s71, s3, s77
	s_add_u32 s76, s69, s84
	s_addc_u32 s77, s71, s85
	s_and_b64 s[8:9], s[8:9], exec
	s_cselect_b32 s9, s77, s83
	s_cselect_b32 s8, s76, s82
	ds_read_b128 v[10:13], v164
	ds_read_b128 v[14:17], v164 offset:1024
	ds_read_b128 v[18:21], v164 offset:2048
	ds_read_b128 v[22:25], v164 offset:3072
	ds_read_b128 v[26:29], v164 offset:4096
	ds_read_b128 v[30:33], v164 offset:5120
	ds_read_b128 v[34:37], v164 offset:6144
	ds_read_b128 v[38:41], v164 offset:7168
	s_waitcnt vmcnt(22)
	s_waitcnt lgkmcnt(0)
	s_barrier
	s_setprio 1
	s_waitcnt lgkmcnt(0)
	v_mfma_f32_16x16x128_f8f6f4 v[130:133], v[2:9], v[10:17], 0
	v_mfma_f32_16x16x128_f8f6f4 v[122:125], v[178:185], v[10:17], 0
	v_mfma_f32_16x16x128_f8f6f4 v[114:117], v[2:9], v[18:25], 0
	v_mfma_f32_16x16x128_f8f6f4 v[106:109], v[178:185], v[18:25], 0
	v_mfma_f32_16x16x128_f8f6f4 v[98:101], v[2:9], v[26:33], 0
	v_mfma_f32_16x16x128_f8f6f4 v[90:93], v[178:185], v[26:33], 0
	v_mfma_f32_16x16x128_f8f6f4 v[74:77], v[2:9], v[34:41], 0
	v_mfma_f32_16x16x128_f8f6f4 v[66:69], v[178:185], v[34:41], 0
	s_setprio 0
	s_setprio 1
	v_mfma_f32_16x16x128_f8f6f4 v[134:137], v[186:193], v[10:17], 0
	v_mfma_f32_16x16x128_f8f6f4 v[126:129], v[194:201], v[10:17], 0
	v_mfma_f32_16x16x128_f8f6f4 v[118:121], v[186:193], v[18:25], 0
	v_mfma_f32_16x16x128_f8f6f4 v[110:113], v[194:201], v[18:25], 0
	v_mfma_f32_16x16x128_f8f6f4 v[102:105], v[186:193], v[26:33], 0
	v_mfma_f32_16x16x128_f8f6f4 v[94:97], v[194:201], v[26:33], 0
	v_mfma_f32_16x16x128_f8f6f4 v[78:81], v[186:193], v[34:41], 0
	v_mfma_f32_16x16x128_f8f6f4 v[70:73], v[194:201], v[34:41], 0
	s_setprio 0
	s_barrier
	s_add_i32 s86, s66, s55
	v_lshl_add_u64 v[156:157], s[82:83], 0, v[138:139]
	s_add_i32 s79, s86, 0x2000
	v_lshl_add_u64 v[10:11], v[156:157], 0, s[40:41]
	s_mov_b32 m0, s86
	v_lshl_add_u64 v[158:159], s[82:83], 0, v[140:141]
	s_add_u32 s84, s82, 0x8100
	ds_read_b128 v[204:207], v164 offset:16384
	ds_read_b128 v[208:211], v164 offset:17408
	ds_read_b128 v[212:215], v164 offset:18432
	ds_read_b128 v[216:219], v164 offset:19456
	ds_read_b128 v[220:223], v164 offset:20480
	ds_read_b128 v[224:227], v164 offset:21504
	ds_read_b128 v[228:231], v164 offset:22528
	ds_read_b128 v[232:235], v164 offset:23552
	global_load_lds_dwordx4 v[10:11], off
	v_lshl_add_u64 v[10:11], v[158:159], 0, s[40:41]
	s_mov_b32 m0, s79
	s_addc_u32 s85, s83, 0
	s_add_i32 s81, s67, s55
	global_load_lds_dwordx4 v[10:11], off
	v_lshl_add_u64 v[10:11], s[84:85], 0, v[138:139]
	s_mov_b32 m0, s81
	s_nop 0
	global_load_lds_dwordx4 v[10:11], off
	v_lshl_add_u64 v[10:11], s[84:85], 0, v[140:141]
	s_add_i32 s84, s81, 0x2000
	s_mov_b32 m0, s84
	s_nop 0
	global_load_lds_dwordx4 v[10:11], off
	s_mov_b32 m0, s57
	s_nop 0
	global_load_lds_dwordx4 v142, s[22:23]
	s_mov_b32 m0, s58
	s_nop 0
	global_load_lds_dwordx4 v154, s[22:23]
	s_waitcnt vmcnt(22)
	s_waitcnt lgkmcnt(0)
	s_barrier
	s_setprio 1
	s_waitcnt lgkmcnt(0)
	v_mfma_f32_16x16x128_f8f6f4 v[58:61], v[2:9], v[204:211], 0
	v_mfma_f32_16x16x128_f8f6f4 v[50:53], v[178:185], v[204:211], 0
	v_mfma_f32_16x16x128_f8f6f4 v[42:45], v[2:9], v[212:219], 0
	v_mfma_f32_16x16x128_f8f6f4 v[34:37], v[178:185], v[212:219], 0
	v_mfma_f32_16x16x128_f8f6f4 v[26:29], v[2:9], v[220:227], 0
	v_mfma_f32_16x16x128_f8f6f4 v[18:21], v[178:185], v[220:227], 0
	v_mfma_f32_16x16x128_f8f6f4 v[10:13], v[2:9], v[228:235], 0
	v_mfma_f32_16x16x128_f8f6f4 v[2:5], v[178:185], v[228:235], 0
	s_setprio 0
	s_setprio 1
	v_mfma_f32_16x16x128_f8f6f4 v[62:65], v[186:193], v[204:211], 0
	v_mfma_f32_16x16x128_f8f6f4 v[54:57], v[194:201], v[204:211], 0
	v_mfma_f32_16x16x128_f8f6f4 v[46:49], v[186:193], v[212:219], 0
	v_mfma_f32_16x16x128_f8f6f4 v[38:41], v[194:201], v[212:219], 0
	v_mfma_f32_16x16x128_f8f6f4 v[30:33], v[186:193], v[220:227], 0
	v_mfma_f32_16x16x128_f8f6f4 v[22:25], v[194:201], v[220:227], 0
	v_mfma_f32_16x16x128_f8f6f4 v[14:17], v[186:193], v[228:235], 0
	v_mfma_f32_16x16x128_f8f6f4 v[6:9], v[194:201], v[228:235], 0
	s_setprio 0
	s_barrier
	s_add_i32 s85, 0, 0x18000
	s_add_i32 s71, 0, 0x1c000
	v_add_u32_e32 v147, s85, v163
	v_add_u32_e32 v149, s71, v163
	ds_read_b128 v[178:181], v147
	ds_read_b128 v[182:185], v147 offset:1024
	ds_read_b128 v[186:189], v147 offset:2048
	ds_read_b128 v[190:193], v147 offset:3072
	ds_read_b128 v[194:197], v149
	ds_read_b128 v[198:201], v149 offset:1024
	ds_read_b128 v[204:207], v149 offset:2048
	ds_read_b128 v[208:211], v149 offset:3072
	s_mov_b32 m0, s59
	ds_read_b128 v[212:215], v164 offset:32768
	ds_read_b128 v[216:219], v164 offset:33792
	ds_read_b128 v[220:223], v164 offset:34816
	ds_read_b128 v[224:227], v164 offset:35840
	ds_read_b128 v[228:231], v164 offset:36864
	ds_read_b128 v[232:235], v164 offset:37888
	ds_read_b128 v[236:239], v164 offset:38912
	ds_read_b128 v[240:243], v164 offset:39936
	global_load_lds_dwordx4 v152, s[22:23]
	s_mov_b32 m0, s60
	s_nop 0
	global_load_lds_dwordx4 v150, s[22:23]
	s_waitcnt vmcnt(22)
	s_waitcnt lgkmcnt(0)
	s_barrier
	s_setprio 1
	s_waitcnt lgkmcnt(0)
	v_mfma_f32_16x16x128_f8f6f4 v[130:133], v[178:185], v[212:219], v[130:133]
	v_mfma_f32_16x16x128_f8f6f4 v[122:125], v[186:193], v[212:219], v[122:125]
	v_mfma_f32_16x16x128_f8f6f4 v[114:117], v[178:185], v[220:227], v[114:117]
	v_mfma_f32_16x16x128_f8f6f4 v[106:109], v[186:193], v[220:227], v[106:109]
	v_mfma_f32_16x16x128_f8f6f4 v[98:101], v[178:185], v[228:235], v[98:101]
	v_mfma_f32_16x16x128_f8f6f4 v[90:93], v[186:193], v[228:235], v[90:93]
	v_mfma_f32_16x16x128_f8f6f4 v[74:77], v[178:185], v[236:243], v[74:77]
	v_mfma_f32_16x16x128_f8f6f4 v[66:69], v[186:193], v[236:243], v[66:69]
	s_setprio 0
	s_setprio 1
	v_mfma_f32_16x16x128_f8f6f4 v[134:137], v[194:201], v[212:219], v[134:137]
	v_mfma_f32_16x16x128_f8f6f4 v[126:129], v[204:211], v[212:219], v[126:129]
	v_mfma_f32_16x16x128_f8f6f4 v[118:121], v[194:201], v[220:227], v[118:121]
	v_mfma_f32_16x16x128_f8f6f4 v[110:113], v[204:211], v[220:227], v[110:113]
	v_mfma_f32_16x16x128_f8f6f4 v[102:105], v[194:201], v[228:235], v[102:105]
	v_mfma_f32_16x16x128_f8f6f4 v[94:97], v[204:211], v[228:235], v[94:97]
	v_mfma_f32_16x16x128_f8f6f4 v[78:81], v[194:201], v[236:243], v[78:81]
	v_mfma_f32_16x16x128_f8f6f4 v[70:73], v[204:211], v[236:243], v[70:73]
	s_setprio 0
	s_barrier
	s_add_i32 s85, s85, s55
	s_add_i32 s69, s85, 0x2000
	v_lshl_add_u64 v[244:245], v[156:157], 0, s[42:43]
	s_mov_b32 m0, s85
	s_add_u32 s88, s82, 0x8180
	ds_read_b128 v[212:215], v164 offset:49152
	ds_read_b128 v[216:219], v164 offset:50176
	ds_read_b128 v[220:223], v164 offset:51200
	ds_read_b128 v[224:227], v164 offset:52224
	ds_read_b128 v[228:231], v164 offset:53248
	ds_read_b128 v[232:235], v164 offset:54272
	ds_read_b128 v[236:239], v164 offset:55296
	ds_read_b128 v[240:243], v164 offset:56320
	global_load_lds_dwordx4 v[244:245], off
	v_lshl_add_u64 v[244:245], v[158:159], 0, s[42:43]
	s_mov_b32 m0, s69
	s_addc_u32 s89, s83, 0
	s_add_i32 s71, s71, s55
	global_load_lds_dwordx4 v[244:245], off
	v_lshl_add_u64 v[244:245], s[88:89], 0, v[138:139]
	s_mov_b32 m0, s71
	s_add_i32 s73, s71, 0x2000
	global_load_lds_dwordx4 v[244:245], off
	v_lshl_add_u64 v[244:245], s[88:89], 0, v[140:141]
	s_mov_b32 m0, s73
	s_nop 0
	global_load_lds_dwordx4 v[244:245], off
	s_mov_b32 m0, s61
	s_nop 0
	global_load_lds_dwordx4 v142, s[24:25]
	s_mov_b32 m0, s62
	s_nop 0
	global_load_lds_dwordx4 v154, s[24:25]
	s_waitcnt vmcnt(8)
	s_waitcnt lgkmcnt(0)
	s_barrier
	s_setprio 1
	s_waitcnt lgkmcnt(0)
	v_mfma_f32_16x16x128_f8f6f4 v[58:61], v[178:185], v[212:219], v[58:61]
	v_mfma_f32_16x16x128_f8f6f4 v[50:53], v[186:193], v[212:219], v[50:53]
	v_mfma_f32_16x16x128_f8f6f4 v[42:45], v[178:185], v[220:227], v[42:45]
	v_mfma_f32_16x16x128_f8f6f4 v[34:37], v[186:193], v[220:227], v[34:37]
	v_mfma_f32_16x16x128_f8f6f4 v[26:29], v[178:185], v[228:235], v[26:29]
	v_mfma_f32_16x16x128_f8f6f4 v[18:21], v[186:193], v[228:235], v[18:21]
	v_mfma_f32_16x16x128_f8f6f4 v[10:13], v[178:185], v[236:243], v[10:13]
	v_mfma_f32_16x16x128_f8f6f4 v[2:5], v[186:193], v[236:243], v[2:5]
	s_setprio 0
	s_setprio 1
	v_mfma_f32_16x16x128_f8f6f4 v[62:65], v[194:201], v[212:219], v[62:65]
	v_mfma_f32_16x16x128_f8f6f4 v[54:57], v[204:211], v[212:219], v[54:57]
	v_mfma_f32_16x16x128_f8f6f4 v[46:49], v[194:201], v[220:227], v[46:49]
	v_mfma_f32_16x16x128_f8f6f4 v[38:41], v[204:211], v[220:227], v[38:41]
	v_mfma_f32_16x16x128_f8f6f4 v[30:33], v[194:201], v[228:235], v[30:33]
	v_mfma_f32_16x16x128_f8f6f4 v[22:25], v[204:211], v[228:235], v[22:25]
	v_mfma_f32_16x16x128_f8f6f4 v[14:17], v[194:201], v[236:243], v[14:17]
	v_mfma_f32_16x16x128_f8f6f4 v[6:9], v[204:211], v[236:243], v[6:9]
	s_setprio 0
	s_barrier
	ds_read_b128 v[178:181], v165
	ds_read_b128 v[182:185], v165 offset:1024
	ds_read_b128 v[186:189], v165 offset:2048
	ds_read_b128 v[190:193], v165 offset:3072
	ds_read_b128 v[194:197], v166
	ds_read_b128 v[198:201], v166 offset:1024
	ds_read_b128 v[204:207], v166 offset:2048
	ds_read_b128 v[208:211], v166 offset:3072
	s_mov_b32 m0, s63
	ds_read_b128 v[212:215], v164
	ds_read_b128 v[216:219], v164 offset:1024
	ds_read_b128 v[220:223], v164 offset:2048
	ds_read_b128 v[224:227], v164 offset:3072
	ds_read_b128 v[228:231], v164 offset:4096
	ds_read_b128 v[232:235], v164 offset:5120
	ds_read_b128 v[236:239], v164 offset:6144
	ds_read_b128 v[240:243], v164 offset:7168
	global_load_lds_dwordx4 v152, s[24:25]
	s_mov_b32 m0, s64
	s_nop 0
	global_load_lds_dwordx4 v150, s[24:25]
	s_waitcnt vmcnt(8)
	s_waitcnt lgkmcnt(0)
	s_barrier
	s_setprio 1
	s_waitcnt lgkmcnt(0)
	v_mfma_f32_16x16x128_f8f6f4 v[130:133], v[178:185], v[212:219], v[130:133]
	v_mfma_f32_16x16x128_f8f6f4 v[122:125], v[186:193], v[212:219], v[122:125]
	v_mfma_f32_16x16x128_f8f6f4 v[114:117], v[178:185], v[220:227], v[114:117]
	v_mfma_f32_16x16x128_f8f6f4 v[106:109], v[186:193], v[220:227], v[106:109]
	v_mfma_f32_16x16x128_f8f6f4 v[98:101], v[178:185], v[228:235], v[98:101]
	v_mfma_f32_16x16x128_f8f6f4 v[90:93], v[186:193], v[228:235], v[90:93]
	v_mfma_f32_16x16x128_f8f6f4 v[74:77], v[178:185], v[236:243], v[74:77]
	v_mfma_f32_16x16x128_f8f6f4 v[66:69], v[186:193], v[236:243], v[66:69]
	s_setprio 0
	s_setprio 1
	v_mfma_f32_16x16x128_f8f6f4 v[134:137], v[194:201], v[212:219], v[134:137]
	v_mfma_f32_16x16x128_f8f6f4 v[126:129], v[204:211], v[212:219], v[126:129]
	v_mfma_f32_16x16x128_f8f6f4 v[118:121], v[194:201], v[220:227], v[118:121]
	v_mfma_f32_16x16x128_f8f6f4 v[110:113], v[204:211], v[220:227], v[110:113]
	v_mfma_f32_16x16x128_f8f6f4 v[102:105], v[194:201], v[228:235], v[102:105]
	v_mfma_f32_16x16x128_f8f6f4 v[94:97], v[204:211], v[228:235], v[94:97]
	v_mfma_f32_16x16x128_f8f6f4 v[78:81], v[194:201], v[236:243], v[78:81]
	v_mfma_f32_16x16x128_f8f6f4 v[70:73], v[204:211], v[236:243], v[70:73]
	s_setprio 0
	s_barrier
	s_mov_b32 m0, s86
	v_lshl_add_u64 v[244:245], v[156:157], 0, s[44:45]
	s_add_u32 s88, s82, 0x8200
	ds_read_b128 v[212:215], v164 offset:16384
	ds_read_b128 v[216:219], v164 offset:17408
	ds_read_b128 v[220:223], v164 offset:18432
	ds_read_b128 v[224:227], v164 offset:19456
	ds_read_b128 v[228:231], v164 offset:20480
	ds_read_b128 v[232:235], v164 offset:21504
	ds_read_b128 v[236:239], v164 offset:22528
	ds_read_b128 v[240:243], v164 offset:23552
	global_load_lds_dwordx4 v[244:245], off
	v_lshl_add_u64 v[244:245], v[158:159], 0, s[44:45]
	s_mov_b32 m0, s79
	s_addc_u32 s89, s83, 0
	global_load_lds_dwordx4 v[244:245], off
	v_lshl_add_u64 v[244:245], s[88:89], 0, v[138:139]
	s_mov_b32 m0, s81
	s_nop 0
	global_load_lds_dwordx4 v[244:245], off
	v_lshl_add_u64 v[244:245], s[88:89], 0, v[140:141]
	s_mov_b32 m0, s84
	s_nop 0
	global_load_lds_dwordx4 v[244:245], off
	s_mov_b32 m0, s57
	s_nop 0
	global_load_lds_dwordx4 v142, s[28:29]
	s_mov_b32 m0, s58
	s_nop 0
	global_load_lds_dwordx4 v154, s[28:29]
	s_waitcnt vmcnt(8)
	s_waitcnt lgkmcnt(0)
	s_barrier
	s_setprio 1
	s_waitcnt lgkmcnt(0)
	v_mfma_f32_16x16x128_f8f6f4 v[58:61], v[178:185], v[212:219], v[58:61]
	v_mfma_f32_16x16x128_f8f6f4 v[50:53], v[186:193], v[212:219], v[50:53]
	v_mfma_f32_16x16x128_f8f6f4 v[42:45], v[178:185], v[220:227], v[42:45]
	v_mfma_f32_16x16x128_f8f6f4 v[34:37], v[186:193], v[220:227], v[34:37]
	v_mfma_f32_16x16x128_f8f6f4 v[26:29], v[178:185], v[228:235], v[26:29]
	v_mfma_f32_16x16x128_f8f6f4 v[18:21], v[186:193], v[228:235], v[18:21]
	v_mfma_f32_16x16x128_f8f6f4 v[10:13], v[178:185], v[236:243], v[10:13]
	v_mfma_f32_16x16x128_f8f6f4 v[2:5], v[186:193], v[236:243], v[2:5]
	s_setprio 0
	s_setprio 1
	v_mfma_f32_16x16x128_f8f6f4 v[62:65], v[194:201], v[212:219], v[62:65]
	v_mfma_f32_16x16x128_f8f6f4 v[54:57], v[204:211], v[212:219], v[54:57]
	v_mfma_f32_16x16x128_f8f6f4 v[46:49], v[194:201], v[220:227], v[46:49]
	v_mfma_f32_16x16x128_f8f6f4 v[38:41], v[204:211], v[220:227], v[38:41]
	v_mfma_f32_16x16x128_f8f6f4 v[30:33], v[194:201], v[228:235], v[30:33]
	v_mfma_f32_16x16x128_f8f6f4 v[22:25], v[204:211], v[228:235], v[22:25]
	v_mfma_f32_16x16x128_f8f6f4 v[14:17], v[194:201], v[236:243], v[14:17]
	v_mfma_f32_16x16x128_f8f6f4 v[6:9], v[204:211], v[236:243], v[6:9]
	s_setprio 0
	s_barrier
	ds_read_b128 v[178:181], v147
	ds_read_b128 v[182:185], v147 offset:1024
	ds_read_b128 v[186:189], v147 offset:2048
	ds_read_b128 v[190:193], v147 offset:3072
	ds_read_b128 v[194:197], v149
	ds_read_b128 v[198:201], v149 offset:1024
	ds_read_b128 v[204:207], v149 offset:2048
	ds_read_b128 v[208:211], v149 offset:3072
	s_mov_b32 m0, s59
	ds_read_b128 v[212:215], v164 offset:32768
	ds_read_b128 v[216:219], v164 offset:33792
	ds_read_b128 v[220:223], v164 offset:34816
	ds_read_b128 v[224:227], v164 offset:35840
	ds_read_b128 v[228:231], v164 offset:36864
	ds_read_b128 v[232:235], v164 offset:37888
	ds_read_b128 v[236:239], v164 offset:38912
	ds_read_b128 v[240:243], v164 offset:39936
	global_load_lds_dwordx4 v152, s[28:29]
	s_mov_b32 m0, s60
	s_nop 0
	global_load_lds_dwordx4 v150, s[28:29]
	s_waitcnt vmcnt(8)
	s_waitcnt lgkmcnt(0)
	s_barrier
	s_setprio 1
	s_waitcnt lgkmcnt(0)
	v_mfma_f32_16x16x128_f8f6f4 v[130:133], v[178:185], v[212:219], v[130:133]
	v_mfma_f32_16x16x128_f8f6f4 v[122:125], v[186:193], v[212:219], v[122:125]
	v_mfma_f32_16x16x128_f8f6f4 v[114:117], v[178:185], v[220:227], v[114:117]
	v_mfma_f32_16x16x128_f8f6f4 v[106:109], v[186:193], v[220:227], v[106:109]
	v_mfma_f32_16x16x128_f8f6f4 v[98:101], v[178:185], v[228:235], v[98:101]
	v_mfma_f32_16x16x128_f8f6f4 v[90:93], v[186:193], v[228:235], v[90:93]
	v_mfma_f32_16x16x128_f8f6f4 v[74:77], v[178:185], v[236:243], v[74:77]
	v_mfma_f32_16x16x128_f8f6f4 v[66:69], v[186:193], v[236:243], v[66:69]
	s_setprio 0
	s_setprio 1
	v_mfma_f32_16x16x128_f8f6f4 v[134:137], v[194:201], v[212:219], v[134:137]
	v_mfma_f32_16x16x128_f8f6f4 v[126:129], v[204:211], v[212:219], v[126:129]
	v_mfma_f32_16x16x128_f8f6f4 v[118:121], v[194:201], v[220:227], v[118:121]
	v_mfma_f32_16x16x128_f8f6f4 v[110:113], v[204:211], v[220:227], v[110:113]
	v_mfma_f32_16x16x128_f8f6f4 v[102:105], v[194:201], v[228:235], v[102:105]
	v_mfma_f32_16x16x128_f8f6f4 v[94:97], v[204:211], v[228:235], v[94:97]
	v_mfma_f32_16x16x128_f8f6f4 v[78:81], v[194:201], v[236:243], v[78:81]
	v_mfma_f32_16x16x128_f8f6f4 v[70:73], v[204:211], v[236:243], v[70:73]
	s_setprio 0
	s_barrier
	s_mov_b32 m0, s85
	v_lshl_add_u64 v[244:245], v[156:157], 0, s[46:47]
	s_add_u32 s88, s82, 0x8280
	ds_read_b128 v[212:215], v164 offset:49152
	ds_read_b128 v[216:219], v164 offset:50176
	ds_read_b128 v[220:223], v164 offset:51200
	ds_read_b128 v[224:227], v164 offset:52224
	ds_read_b128 v[228:231], v164 offset:53248
	ds_read_b128 v[232:235], v164 offset:54272
	ds_read_b128 v[236:239], v164 offset:55296
	ds_read_b128 v[240:243], v164 offset:56320
	global_load_lds_dwordx4 v[244:245], off
	v_lshl_add_u64 v[244:245], v[158:159], 0, s[46:47]
	s_mov_b32 m0, s69
	s_addc_u32 s89, s83, 0
	global_load_lds_dwordx4 v[244:245], off
	v_lshl_add_u64 v[244:245], s[88:89], 0, v[138:139]
	s_mov_b32 m0, s71
	s_nop 0
	global_load_lds_dwordx4 v[244:245], off
	v_lshl_add_u64 v[244:245], s[88:89], 0, v[140:141]
	s_mov_b32 m0, s73
	s_nop 0
	global_load_lds_dwordx4 v[244:245], off
	s_mov_b32 m0, s61
	s_nop 0
	global_load_lds_dwordx4 v142, s[30:31]
	s_mov_b32 m0, s62
	s_nop 0
	global_load_lds_dwordx4 v154, s[30:31]
	s_waitcnt vmcnt(8)
	s_waitcnt lgkmcnt(0)
	s_barrier
	s_setprio 1
	s_waitcnt lgkmcnt(0)
	v_mfma_f32_16x16x128_f8f6f4 v[58:61], v[178:185], v[212:219], v[58:61]
	v_mfma_f32_16x16x128_f8f6f4 v[50:53], v[186:193], v[212:219], v[50:53]
	v_mfma_f32_16x16x128_f8f6f4 v[42:45], v[178:185], v[220:227], v[42:45]
	v_mfma_f32_16x16x128_f8f6f4 v[34:37], v[186:193], v[220:227], v[34:37]
	v_mfma_f32_16x16x128_f8f6f4 v[26:29], v[178:185], v[228:235], v[26:29]
	v_mfma_f32_16x16x128_f8f6f4 v[18:21], v[186:193], v[228:235], v[18:21]
	v_mfma_f32_16x16x128_f8f6f4 v[10:13], v[178:185], v[236:243], v[10:13]
	v_mfma_f32_16x16x128_f8f6f4 v[2:5], v[186:193], v[236:243], v[2:5]
	s_setprio 0
	s_setprio 1
	v_mfma_f32_16x16x128_f8f6f4 v[62:65], v[194:201], v[212:219], v[62:65]
	v_mfma_f32_16x16x128_f8f6f4 v[54:57], v[204:211], v[212:219], v[54:57]
	v_mfma_f32_16x16x128_f8f6f4 v[46:49], v[194:201], v[220:227], v[46:49]
	v_mfma_f32_16x16x128_f8f6f4 v[38:41], v[204:211], v[220:227], v[38:41]
	v_mfma_f32_16x16x128_f8f6f4 v[30:33], v[194:201], v[228:235], v[30:33]
	v_mfma_f32_16x16x128_f8f6f4 v[22:25], v[204:211], v[228:235], v[22:25]
	v_mfma_f32_16x16x128_f8f6f4 v[14:17], v[194:201], v[236:243], v[14:17]
	v_mfma_f32_16x16x128_f8f6f4 v[6:9], v[204:211], v[236:243], v[6:9]
	s_setprio 0
	s_barrier
	ds_read_b128 v[178:181], v165
	ds_read_b128 v[182:185], v165 offset:1024
	ds_read_b128 v[186:189], v165 offset:2048
	ds_read_b128 v[190:193], v165 offset:3072
	ds_read_b128 v[194:197], v166
	ds_read_b128 v[198:201], v166 offset:1024
	ds_read_b128 v[204:207], v166 offset:2048
	ds_read_b128 v[208:211], v166 offset:3072
	s_mov_b32 m0, s63
	ds_read_b128 v[212:215], v164
	ds_read_b128 v[216:219], v164 offset:1024
	ds_read_b128 v[220:223], v164 offset:2048
	ds_read_b128 v[224:227], v164 offset:3072
	ds_read_b128 v[228:231], v164 offset:4096
	ds_read_b128 v[232:235], v164 offset:5120
	ds_read_b128 v[236:239], v164 offset:6144
	ds_read_b128 v[240:243], v164 offset:7168
	global_load_lds_dwordx4 v152, s[30:31]
	s_mov_b32 m0, s64
	s_nop 0
	global_load_lds_dwordx4 v150, s[30:31]
	s_waitcnt vmcnt(8)
	s_waitcnt lgkmcnt(0)
	s_barrier
	s_setprio 1
	s_waitcnt lgkmcnt(0)
	v_mfma_f32_16x16x128_f8f6f4 v[130:133], v[178:185], v[212:219], v[130:133]
	v_mfma_f32_16x16x128_f8f6f4 v[122:125], v[186:193], v[212:219], v[122:125]
	v_mfma_f32_16x16x128_f8f6f4 v[114:117], v[178:185], v[220:227], v[114:117]
	v_mfma_f32_16x16x128_f8f6f4 v[106:109], v[186:193], v[220:227], v[106:109]
	v_mfma_f32_16x16x128_f8f6f4 v[98:101], v[178:185], v[228:235], v[98:101]
	v_mfma_f32_16x16x128_f8f6f4 v[90:93], v[186:193], v[228:235], v[90:93]
	v_mfma_f32_16x16x128_f8f6f4 v[74:77], v[178:185], v[236:243], v[74:77]
	v_mfma_f32_16x16x128_f8f6f4 v[66:69], v[186:193], v[236:243], v[66:69]
	s_setprio 0
	s_setprio 1
	v_mfma_f32_16x16x128_f8f6f4 v[134:137], v[194:201], v[212:219], v[134:137]
	v_mfma_f32_16x16x128_f8f6f4 v[126:129], v[204:211], v[212:219], v[126:129]
	v_mfma_f32_16x16x128_f8f6f4 v[118:121], v[194:201], v[220:227], v[118:121]
	v_mfma_f32_16x16x128_f8f6f4 v[110:113], v[204:211], v[220:227], v[110:113]
	v_mfma_f32_16x16x128_f8f6f4 v[102:105], v[194:201], v[228:235], v[102:105]
	v_mfma_f32_16x16x128_f8f6f4 v[94:97], v[204:211], v[228:235], v[94:97]
	v_mfma_f32_16x16x128_f8f6f4 v[78:81], v[194:201], v[236:243], v[78:81]
	v_mfma_f32_16x16x128_f8f6f4 v[70:73], v[204:211], v[236:243], v[70:73]
	s_setprio 0
	s_barrier
	s_mov_b32 m0, s86
	v_lshl_add_u64 v[244:245], v[156:157], 0, s[48:49]
	s_add_u32 s88, s82, 0x8300
	ds_read_b128 v[212:215], v164 offset:16384
	ds_read_b128 v[216:219], v164 offset:17408
	ds_read_b128 v[220:223], v164 offset:18432
	ds_read_b128 v[224:227], v164 offset:19456
	ds_read_b128 v[228:231], v164 offset:20480
	ds_read_b128 v[232:235], v164 offset:21504
	ds_read_b128 v[236:239], v164 offset:22528
	ds_read_b128 v[240:243], v164 offset:23552
	global_load_lds_dwordx4 v[244:245], off
	v_lshl_add_u64 v[244:245], v[158:159], 0, s[48:49]
	s_mov_b32 m0, s79
	s_addc_u32 s89, s83, 0
	global_load_lds_dwordx4 v[244:245], off
	v_lshl_add_u64 v[244:245], s[88:89], 0, v[138:139]
	s_mov_b32 m0, s81
	s_nop 0
	global_load_lds_dwordx4 v[244:245], off
	v_lshl_add_u64 v[244:245], s[88:89], 0, v[140:141]
	s_mov_b32 m0, s84
	s_nop 0
	global_load_lds_dwordx4 v[244:245], off
	s_mov_b32 m0, s57
	s_nop 0
	global_load_lds_dwordx4 v142, s[34:35]
	s_mov_b32 m0, s58
	s_nop 0
	global_load_lds_dwordx4 v154, s[34:35]
	s_waitcnt vmcnt(8)
	s_waitcnt lgkmcnt(0)
	s_barrier
	s_setprio 1
	s_waitcnt lgkmcnt(0)
	v_mfma_f32_16x16x128_f8f6f4 v[58:61], v[178:185], v[212:219], v[58:61]
	v_mfma_f32_16x16x128_f8f6f4 v[50:53], v[186:193], v[212:219], v[50:53]
	v_mfma_f32_16x16x128_f8f6f4 v[42:45], v[178:185], v[220:227], v[42:45]
	v_mfma_f32_16x16x128_f8f6f4 v[34:37], v[186:193], v[220:227], v[34:37]
	v_mfma_f32_16x16x128_f8f6f4 v[26:29], v[178:185], v[228:235], v[26:29]
	v_mfma_f32_16x16x128_f8f6f4 v[18:21], v[186:193], v[228:235], v[18:21]
	v_mfma_f32_16x16x128_f8f6f4 v[10:13], v[178:185], v[236:243], v[10:13]
	v_mfma_f32_16x16x128_f8f6f4 v[2:5], v[186:193], v[236:243], v[2:5]
	s_setprio 0
	s_setprio 1
	v_mfma_f32_16x16x128_f8f6f4 v[62:65], v[194:201], v[212:219], v[62:65]
	v_mfma_f32_16x16x128_f8f6f4 v[54:57], v[204:211], v[212:219], v[54:57]
	v_mfma_f32_16x16x128_f8f6f4 v[46:49], v[194:201], v[220:227], v[46:49]
	v_mfma_f32_16x16x128_f8f6f4 v[38:41], v[204:211], v[220:227], v[38:41]
	v_mfma_f32_16x16x128_f8f6f4 v[30:33], v[194:201], v[228:235], v[30:33]
	v_mfma_f32_16x16x128_f8f6f4 v[22:25], v[204:211], v[228:235], v[22:25]
	v_mfma_f32_16x16x128_f8f6f4 v[14:17], v[194:201], v[236:243], v[14:17]
	v_mfma_f32_16x16x128_f8f6f4 v[6:9], v[204:211], v[236:243], v[6:9]
	s_setprio 0
	s_barrier
	ds_read_b128 v[178:181], v147
	ds_read_b128 v[182:185], v147 offset:1024
	ds_read_b128 v[186:189], v147 offset:2048
	ds_read_b128 v[190:193], v147 offset:3072
	ds_read_b128 v[194:197], v149
	ds_read_b128 v[198:201], v149 offset:1024
	ds_read_b128 v[204:207], v149 offset:2048
	ds_read_b128 v[208:211], v149 offset:3072
	s_mov_b32 m0, s59
	ds_read_b128 v[212:215], v164 offset:32768
	ds_read_b128 v[216:219], v164 offset:33792
	ds_read_b128 v[220:223], v164 offset:34816
	ds_read_b128 v[224:227], v164 offset:35840
	ds_read_b128 v[228:231], v164 offset:36864
	ds_read_b128 v[232:235], v164 offset:37888
	ds_read_b128 v[236:239], v164 offset:38912
	ds_read_b128 v[240:243], v164 offset:39936
	global_load_lds_dwordx4 v152, s[34:35]
	s_mov_b32 m0, s60
	s_nop 0
	global_load_lds_dwordx4 v150, s[34:35]
	s_waitcnt vmcnt(8)
	s_waitcnt lgkmcnt(0)
	s_barrier
	s_setprio 1
	s_waitcnt lgkmcnt(0)
	v_mfma_f32_16x16x128_f8f6f4 v[130:133], v[178:185], v[212:219], v[130:133]
	v_mfma_f32_16x16x128_f8f6f4 v[122:125], v[186:193], v[212:219], v[122:125]
	v_mfma_f32_16x16x128_f8f6f4 v[114:117], v[178:185], v[220:227], v[114:117]
	v_mfma_f32_16x16x128_f8f6f4 v[106:109], v[186:193], v[220:227], v[106:109]
	v_mfma_f32_16x16x128_f8f6f4 v[98:101], v[178:185], v[228:235], v[98:101]
	v_mfma_f32_16x16x128_f8f6f4 v[90:93], v[186:193], v[228:235], v[90:93]
	v_mfma_f32_16x16x128_f8f6f4 v[74:77], v[178:185], v[236:243], v[74:77]
	v_mfma_f32_16x16x128_f8f6f4 v[66:69], v[186:193], v[236:243], v[66:69]
	s_setprio 0
	s_setprio 1
	v_mfma_f32_16x16x128_f8f6f4 v[134:137], v[194:201], v[212:219], v[134:137]
	v_mfma_f32_16x16x128_f8f6f4 v[126:129], v[204:211], v[212:219], v[126:129]
	v_mfma_f32_16x16x128_f8f6f4 v[118:121], v[194:201], v[220:227], v[118:121]
	v_mfma_f32_16x16x128_f8f6f4 v[110:113], v[204:211], v[220:227], v[110:113]
	v_mfma_f32_16x16x128_f8f6f4 v[102:105], v[194:201], v[228:235], v[102:105]
	v_mfma_f32_16x16x128_f8f6f4 v[94:97], v[204:211], v[228:235], v[94:97]
	v_mfma_f32_16x16x128_f8f6f4 v[78:81], v[194:201], v[236:243], v[78:81]
	v_mfma_f32_16x16x128_f8f6f4 v[70:73], v[204:211], v[236:243], v[70:73]
	s_setprio 0
	s_barrier
	s_mov_b32 m0, s85
	v_lshl_add_u64 v[156:157], v[156:157], 0, s[50:51]
	s_add_u32 s82, s82, 0x8380
	ds_read_b128 v[212:215], v164 offset:49152
	ds_read_b128 v[216:219], v164 offset:50176
	ds_read_b128 v[220:223], v164 offset:51200
	ds_read_b128 v[224:227], v164 offset:52224
	ds_read_b128 v[228:231], v164 offset:53248
	ds_read_b128 v[232:235], v164 offset:54272
	ds_read_b128 v[236:239], v164 offset:55296
	ds_read_b128 v[240:243], v164 offset:56320
	global_load_lds_dwordx4 v[156:157], off
	v_lshl_add_u64 v[156:157], v[158:159], 0, s[50:51]
	s_mov_b32 m0, s69
	s_addc_u32 s83, s83, 0
	global_load_lds_dwordx4 v[156:157], off
	v_lshl_add_u64 v[156:157], s[82:83], 0, v[138:139]
	s_mov_b32 m0, s71
	s_nop 0
	global_load_lds_dwordx4 v[156:157], off
	v_lshl_add_u64 v[156:157], s[82:83], 0, v[140:141]
	s_mov_b32 m0, s73
	s_nop 0
	global_load_lds_dwordx4 v[156:157], off
	s_mov_b32 m0, s61
	s_nop 0
	global_load_lds_dwordx4 v142, s[36:37]
	s_mov_b32 m0, s62
	s_nop 0
	global_load_lds_dwordx4 v154, s[36:37]
	s_waitcnt vmcnt(8)
	s_waitcnt lgkmcnt(0)
	s_barrier
	s_setprio 1
	s_waitcnt lgkmcnt(0)
	v_mfma_f32_16x16x128_f8f6f4 v[58:61], v[178:185], v[212:219], v[58:61]
	v_mfma_f32_16x16x128_f8f6f4 v[50:53], v[186:193], v[212:219], v[50:53]
	v_mfma_f32_16x16x128_f8f6f4 v[42:45], v[178:185], v[220:227], v[42:45]
	v_mfma_f32_16x16x128_f8f6f4 v[34:37], v[186:193], v[220:227], v[34:37]
	v_mfma_f32_16x16x128_f8f6f4 v[26:29], v[178:185], v[228:235], v[26:29]
	v_mfma_f32_16x16x128_f8f6f4 v[18:21], v[186:193], v[228:235], v[18:21]
	v_mfma_f32_16x16x128_f8f6f4 v[10:13], v[178:185], v[236:243], v[10:13]
	v_mfma_f32_16x16x128_f8f6f4 v[2:5], v[186:193], v[236:243], v[2:5]
	s_setprio 0
	s_setprio 1
	v_mfma_f32_16x16x128_f8f6f4 v[62:65], v[194:201], v[212:219], v[62:65]
	v_mfma_f32_16x16x128_f8f6f4 v[54:57], v[204:211], v[212:219], v[54:57]
	v_mfma_f32_16x16x128_f8f6f4 v[46:49], v[194:201], v[220:227], v[46:49]
	v_mfma_f32_16x16x128_f8f6f4 v[38:41], v[204:211], v[220:227], v[38:41]
	v_mfma_f32_16x16x128_f8f6f4 v[30:33], v[194:201], v[228:235], v[30:33]
	v_mfma_f32_16x16x128_f8f6f4 v[22:25], v[204:211], v[228:235], v[22:25]
	v_mfma_f32_16x16x128_f8f6f4 v[14:17], v[194:201], v[236:243], v[14:17]
	v_mfma_f32_16x16x128_f8f6f4 v[6:9], v[204:211], v[236:243], v[6:9]
	s_setprio 0
	s_barrier
	ds_read_b128 v[178:181], v165
	ds_read_b128 v[182:185], v165 offset:1024
	ds_read_b128 v[186:189], v165 offset:2048
	ds_read_b128 v[190:193], v165 offset:3072
	ds_read_b128 v[194:197], v166
	ds_read_b128 v[198:201], v166 offset:1024
	ds_read_b128 v[204:207], v166 offset:2048
	ds_read_b128 v[208:211], v166 offset:3072
	s_mov_b32 m0, s63
	ds_read_b128 v[212:215], v164
	ds_read_b128 v[216:219], v164 offset:1024
	ds_read_b128 v[220:223], v164 offset:2048
	ds_read_b128 v[224:227], v164 offset:3072
	ds_read_b128 v[228:231], v164 offset:4096
	ds_read_b128 v[232:235], v164 offset:5120
	ds_read_b128 v[236:239], v164 offset:6144
	ds_read_b128 v[240:243], v164 offset:7168
	global_load_lds_dwordx4 v152, s[36:37]
	s_mov_b32 m0, s64
	s_nop 0
	global_load_lds_dwordx4 v150, s[36:37]
	s_waitcnt vmcnt(8)
	s_waitcnt lgkmcnt(0)
	s_barrier
	s_setprio 1
	s_waitcnt lgkmcnt(0)
	v_mfma_f32_16x16x128_f8f6f4 v[130:133], v[178:185], v[212:219], v[130:133]
	v_mfma_f32_16x16x128_f8f6f4 v[122:125], v[186:193], v[212:219], v[122:125]
	v_mfma_f32_16x16x128_f8f6f4 v[114:117], v[178:185], v[220:227], v[114:117]
	v_mfma_f32_16x16x128_f8f6f4 v[106:109], v[186:193], v[220:227], v[106:109]
	v_mfma_f32_16x16x128_f8f6f4 v[98:101], v[178:185], v[228:235], v[98:101]
	v_mfma_f32_16x16x128_f8f6f4 v[90:93], v[186:193], v[228:235], v[90:93]
	v_mfma_f32_16x16x128_f8f6f4 v[74:77], v[178:185], v[236:243], v[74:77]
	v_mfma_f32_16x16x128_f8f6f4 v[66:69], v[186:193], v[236:243], v[66:69]
	s_setprio 0
	s_setprio 1
	v_mfma_f32_16x16x128_f8f6f4 v[134:137], v[194:201], v[212:219], v[134:137]
	v_mfma_f32_16x16x128_f8f6f4 v[126:129], v[204:211], v[212:219], v[126:129]
	v_mfma_f32_16x16x128_f8f6f4 v[118:121], v[194:201], v[220:227], v[118:121]
	v_mfma_f32_16x16x128_f8f6f4 v[110:113], v[204:211], v[220:227], v[110:113]
	v_mfma_f32_16x16x128_f8f6f4 v[102:105], v[194:201], v[228:235], v[102:105]
	v_mfma_f32_16x16x128_f8f6f4 v[94:97], v[204:211], v[228:235], v[94:97]
	v_mfma_f32_16x16x128_f8f6f4 v[78:81], v[194:201], v[236:243], v[78:81]
	v_mfma_f32_16x16x128_f8f6f4 v[70:73], v[204:211], v[236:243], v[70:73]
	s_setprio 0
	s_barrier
	s_cmp_lg_u64 s[6:7], 0
	s_cbranch_scc1 .Lgu0_rm_skip
	v_lshlrev_b32_e32 v246, 10, v246
	v_lshlrev_b32_e32 v247, 10, v247
	v_lshlrev_b32_e32 v248, 10, v248
	v_lshlrev_b32_e32 v249, 10, v249
	v_and_b32_e32 v246, 0x3fffc00, v246
	v_and_b32_e32 v247, 0x3fffc00, v247
	v_and_b32_e32 v249, 0x3fffc00, v249
	v_and_b32_e32 v248, 0x3fffc00, v248
	v_add_u32_e32 v169, v246, v161
	v_add_u32_e32 v170, v247, v162
	v_add_u32_e32 v146, v249, v161
	v_add_u32_e32 v148, v248, v162
.Lgu0_rm_skip:
	s_mov_b32 m0, s86
	v_lshl_add_u64 v[158:159], s[8:9], 0, v[138:139]
	s_add_u32 s82, s8, 0x8000
	ds_read_b128 v[150:153], v164 offset:16384
	ds_read_b128 v[154:157], v164 offset:17408
	ds_read_b128 v[212:215], v164 offset:18432
	ds_read_b128 v[216:219], v164 offset:19456
	ds_read_b128 v[220:223], v164 offset:20480
	ds_read_b128 v[224:227], v164 offset:21504
	ds_read_b128 v[228:231], v164 offset:22528
	ds_read_b128 v[232:235], v164 offset:23552
	global_load_lds_dwordx4 v[158:159], off
	v_lshl_add_u64 v[236:237], s[8:9], 0, v[140:141]
	s_mov_b32 m0, s79
	s_addc_u32 s83, s9, 0
	global_load_lds_dwordx4 v[236:237], off
	v_lshl_add_u64 v[238:239], s[82:83], 0, v[138:139]
	s_mov_b32 m0, s81
	s_nop 0
	global_load_lds_dwordx4 v[238:239], off
	v_lshl_add_u64 v[238:239], s[82:83], 0, v[140:141]
	s_mov_b32 m0, s84
	s_nop 0
	global_load_lds_dwordx4 v[238:239], off
	s_mov_b32 m0, s57
	s_nop 0
	global_load_lds_dwordx4 v169, s[10:11]
	s_mov_b32 m0, s58
	s_nop 0
	global_load_lds_dwordx4 v170, s[10:11]
	s_waitcnt vmcnt(8)
	s_waitcnt lgkmcnt(0)
	s_barrier
	s_setprio 1
	s_waitcnt lgkmcnt(0)
	v_mfma_f32_16x16x128_f8f6f4 v[58:61], v[178:185], v[150:157], v[58:61]
	v_mfma_f32_16x16x128_f8f6f4 v[50:53], v[186:193], v[150:157], v[50:53]
	v_mfma_f32_16x16x128_f8f6f4 v[42:45], v[178:185], v[212:219], v[42:45]
	v_mfma_f32_16x16x128_f8f6f4 v[34:37], v[186:193], v[212:219], v[34:37]
	v_mfma_f32_16x16x128_f8f6f4 v[26:29], v[178:185], v[220:227], v[26:29]
	v_mfma_f32_16x16x128_f8f6f4 v[18:21], v[186:193], v[220:227], v[18:21]
	v_mfma_f32_16x16x128_f8f6f4 v[10:13], v[178:185], v[228:235], v[10:13]
	v_mfma_f32_16x16x128_f8f6f4 v[2:5], v[186:193], v[228:235], v[2:5]
	s_setprio 0
	s_setprio 1
	v_mfma_f32_16x16x128_f8f6f4 v[62:65], v[194:201], v[150:157], v[62:65]
	v_mfma_f32_16x16x128_f8f6f4 v[54:57], v[204:211], v[150:157], v[54:57]
	v_mfma_f32_16x16x128_f8f6f4 v[46:49], v[194:201], v[212:219], v[46:49]
	v_mfma_f32_16x16x128_f8f6f4 v[38:41], v[204:211], v[212:219], v[38:41]
	v_mfma_f32_16x16x128_f8f6f4 v[30:33], v[194:201], v[220:227], v[30:33]
	v_mfma_f32_16x16x128_f8f6f4 v[22:25], v[204:211], v[220:227], v[22:25]
	v_mfma_f32_16x16x128_f8f6f4 v[14:17], v[194:201], v[228:235], v[14:17]
	v_mfma_f32_16x16x128_f8f6f4 v[6:9], v[204:211], v[228:235], v[6:9]
	s_setprio 0
	s_barrier
	ds_read_b128 v[150:153], v147
	ds_read_b128 v[154:157], v147 offset:1024
	ds_read_b128 v[178:181], v147 offset:2048
	ds_read_b128 v[182:185], v147 offset:3072
	ds_read_b128 v[186:189], v149
	ds_read_b128 v[190:193], v149 offset:1024
	ds_read_b128 v[194:197], v149 offset:2048
	ds_read_b128 v[198:201], v149 offset:3072
	s_mov_b32 m0, s59
	ds_read_b128 v[204:207], v164 offset:32768
	ds_read_b128 v[208:211], v164 offset:33792
	ds_read_b128 v[212:215], v164 offset:34816
	ds_read_b128 v[216:219], v164 offset:35840
	ds_read_b128 v[220:223], v164 offset:36864
	ds_read_b128 v[224:227], v164 offset:37888
	ds_read_b128 v[228:231], v164 offset:38912
	ds_read_b128 v[232:235], v164 offset:39936
	global_load_lds_dwordx4 v146, s[10:11]
	s_mov_b32 m0, s60
	s_nop 0
	global_load_lds_dwordx4 v148, s[10:11]
	s_waitcnt vmcnt(8)
	s_waitcnt lgkmcnt(0)
	s_barrier
	s_setprio 1
	s_waitcnt lgkmcnt(0)
	v_mfma_f32_16x16x128_f8f6f4 v[130:133], v[150:157], v[204:211], v[130:133]
	v_mfma_f32_16x16x128_f8f6f4 v[122:125], v[178:185], v[204:211], v[122:125]
	v_mfma_f32_16x16x128_f8f6f4 v[114:117], v[150:157], v[212:219], v[114:117]
	v_mfma_f32_16x16x128_f8f6f4 v[106:109], v[178:185], v[212:219], v[106:109]
	v_mfma_f32_16x16x128_f8f6f4 v[98:101], v[150:157], v[220:227], v[98:101]
	v_mfma_f32_16x16x128_f8f6f4 v[90:93], v[178:185], v[220:227], v[90:93]
	v_mfma_f32_16x16x128_f8f6f4 v[74:77], v[150:157], v[228:235], v[74:77]
	v_mfma_f32_16x16x128_f8f6f4 v[66:69], v[178:185], v[228:235], v[66:69]
	s_setprio 0
	s_setprio 1
	v_mfma_f32_16x16x128_f8f6f4 v[134:137], v[186:193], v[204:211], v[134:137]
	v_mfma_f32_16x16x128_f8f6f4 v[126:129], v[194:201], v[204:211], v[126:129]
	v_mfma_f32_16x16x128_f8f6f4 v[118:121], v[186:193], v[212:219], v[118:121]
	v_mfma_f32_16x16x128_f8f6f4 v[110:113], v[194:201], v[212:219], v[110:113]
	v_mfma_f32_16x16x128_f8f6f4 v[102:105], v[186:193], v[220:227], v[102:105]
	v_mfma_f32_16x16x128_f8f6f4 v[94:97], v[194:201], v[220:227], v[94:97]
	v_mfma_f32_16x16x128_f8f6f4 v[78:81], v[186:193], v[228:235], v[78:81]
	v_mfma_f32_16x16x128_f8f6f4 v[70:73], v[194:201], v[228:235], v[70:73]
	s_setprio 0
	s_barrier
	s_mov_b32 m0, s85
	v_lshl_add_u64 v[158:159], v[158:159], 0, s[18:19]
	s_add_u32 s8, s8, 0x8080
	ds_read_b128 v[204:207], v164 offset:49152
	ds_read_b128 v[208:211], v164 offset:50176
	ds_read_b128 v[212:215], v164 offset:51200
	ds_read_b128 v[216:219], v164 offset:52224
	ds_read_b128 v[220:223], v164 offset:53248
	ds_read_b128 v[224:227], v164 offset:54272
	ds_read_b128 v[228:231], v164 offset:55296
	ds_read_b128 v[232:235], v164 offset:56320
	global_load_lds_dwordx4 v[158:159], off
	v_lshl_add_u64 v[158:159], v[236:237], 0, s[18:19]
	s_mov_b32 m0, s69
	s_addc_u32 s9, s9, 0
	global_load_lds_dwordx4 v[158:159], off
	v_lshl_add_u64 v[158:159], s[8:9], 0, v[138:139]
	s_mov_b32 m0, s71
	s_nop 0
	global_load_lds_dwordx4 v[158:159], off
	v_lshl_add_u64 v[158:159], s[8:9], 0, v[140:141]
	s_mov_b32 m0, s73
	s_nop 0
	global_load_lds_dwordx4 v[158:159], off
	s_mov_b32 m0, s61
	s_nop 0
	global_load_lds_dwordx4 v169, s[20:21]
	s_mov_b32 m0, s62
	s_nop 0
	global_load_lds_dwordx4 v170, s[20:21]
	s_waitcnt vmcnt(8)
	s_waitcnt lgkmcnt(0)
	s_barrier
	s_setprio 1
	s_waitcnt lgkmcnt(0)
	v_mfma_f32_16x16x128_f8f6f4 v[58:61], v[150:157], v[204:211], v[58:61]
	v_mfma_f32_16x16x128_f8f6f4 v[50:53], v[178:185], v[204:211], v[50:53]
	v_mfma_f32_16x16x128_f8f6f4 v[42:45], v[150:157], v[212:219], v[42:45]
	v_mfma_f32_16x16x128_f8f6f4 v[34:37], v[178:185], v[212:219], v[34:37]
	v_mfma_f32_16x16x128_f8f6f4 v[26:29], v[150:157], v[220:227], v[26:29]
	v_mfma_f32_16x16x128_f8f6f4 v[18:21], v[178:185], v[220:227], v[18:21]
	v_mfma_f32_16x16x128_f8f6f4 v[10:13], v[150:157], v[228:235], v[10:13]
	v_mfma_f32_16x16x128_f8f6f4 v[2:5], v[178:185], v[228:235], v[2:5]
	s_setprio 0
	s_setprio 1
	v_mfma_f32_16x16x128_f8f6f4 v[62:65], v[186:193], v[204:211], v[62:65]
	v_mfma_f32_16x16x128_f8f6f4 v[54:57], v[194:201], v[204:211], v[54:57]
	v_mfma_f32_16x16x128_f8f6f4 v[46:49], v[186:193], v[212:219], v[46:49]
	v_mfma_f32_16x16x128_f8f6f4 v[38:41], v[194:201], v[212:219], v[38:41]
	v_mfma_f32_16x16x128_f8f6f4 v[30:33], v[186:193], v[220:227], v[30:33]
	v_mfma_f32_16x16x128_f8f6f4 v[22:25], v[194:201], v[220:227], v[22:25]
	v_mfma_f32_16x16x128_f8f6f4 v[14:17], v[186:193], v[228:235], v[14:17]
	v_mfma_f32_16x16x128_f8f6f4 v[6:9], v[194:201], v[228:235], v[6:9]
	s_setprio 0
	s_barrier
	s_and_b64 vcc, exec, s[6:7]
	s_cbranch_vccnz .LBB0_1544
	v_mov_b32_e32 v147, v143
	s_mov_b32 m0, s63
	v_mov_b32_e32 v149, v143
	v_lshl_add_u64 v[150:151], s[20:21], 0, v[146:147]
	v_lshl_add_u64 v[152:153], s[20:21], 0, v[148:149]
	global_load_lds_dwordx4 v[150:151], off
	s_mov_b32 m0, s64
	s_nop 0
	global_load_lds_dwordx4 v[152:153], off
